# P18 final pass: the wave's 32 expert-slot words preloaded once (one coalesced load + v_readlane) instead of four dependent single-dword loads per row pair
# speedup vs baseline: 1.0077x; 1.0007x over previous
.LBB0_2296:
	s_cmp_lt_i32 s74, 19
	s_cselect_b64 s[0:1], -1, 0
	s_and_b64 s[0:1], s[0:1], s[2:3]
	s_andn2_b64 vcc, exec, s[0:1]
	s_cbranch_vccnz .LBB0_2310
	v_readlane_b32 s2, v254, 9
	s_abs_i32 s0, s2
	v_cvt_f32_u32_e32 v0, s0
	s_sub_i32 s3, 0, s0
	s_add_i32 s1, s2, 0x7fff
	s_xor_b32 s2, s1, s2
	v_rcp_iflag_f32_e32 v0, v0
	s_abs_i32 s1, s1
	s_ashr_i32 s2, s2, 31
	v_mul_f32_e32 v0, 0x4f7ffffe, v0
	v_cvt_u32_f32_e32 v0, v0
	s_nop 0
	v_readfirstlane_b32 s4, v0
	s_mul_i32 s3, s3, s4
	s_mul_hi_u32 s3, s4, s3
	s_add_i32 s4, s4, s3
	s_mul_hi_u32 s3, s1, s4
	s_mul_i32 s4, s3, s0
	s_sub_i32 s1, s1, s4
	s_add_i32 s5, s3, 1
	s_sub_i32 s4, s1, s0
	s_cmp_ge_u32 s1, s0
	s_cselect_b32 s3, s5, s3
	s_cselect_b32 s1, s4, s1
	s_add_i32 s4, s3, 1
	s_cmp_ge_u32 s1, s0
	s_cselect_b32 s0, s4, s3
	s_xor_b32 s0, s0, s2
	s_sub_i32 s1, s0, s2
	s_add_i32 s1, s1, 1
	s_and_b32 s0, s1, -2
	s_mul_i32 s2, s0, s97
	s_add_i32 s0, s2, s0
	s_min_i32 s18, s0, 0x8000
	s_cmp_ge_i32 s2, s18
	s_mov_b32 s0, 0
	s_cbranch_scc1 .LBB0_2310
	s_waitcnt vmcnt(0) lgkmcnt(0)
	v_lshlrev_b32_e32 v16, 4, v250
	global_load_dwordx4 v[0:3], v16, s[68:69]
	global_load_dwordx4 v[4:7], v16, s[68:69] offset:1024
	global_load_dwordx4 v[8:11], v16, s[68:69] offset:2048
	global_load_dwordx4 v[12:15], v16, s[68:69] offset:3072
	s_lshl_b32 s19, s31, 14
	s_add_u32 s20, s72, 0x180000
	s_addc_u32 s21, s73, 0
	s_add_u32 s22, s72, 0x140000
	s_addc_u32 s23, s73, 0
	s_cmp_le_i32 s28, s6
	v_lshlrev_b32_e32 v32, 2, v250
	v_mov_b32_e32 v33, 0
	s_cselect_b64 s[4:5], -1, 0
	s_lshr_b32 s1, s1, 1
	v_lshl_add_u64 v[24:25], s[72:73], 0, v[32:33]
	s_mov_b64 s[6:7], 0xdd00000
	s_mul_i32 s1, s1, s97
	s_ashr_i32 s3, s2, 31
	v_lshl_add_u64 v[34:35], v[24:25], 0, s[6:7]
	s_lshl_b32 s6, s1, 2
	s_lshl_b64 s[8:9], s[2:3], 11
	s_add_u32 s8, s72, s8
	v_lshlrev_b32_e32 v24, 3, v250
	v_mov_b32_e32 v25, v33
	s_addc_u32 s9, s73, s9
	v_lshl_add_u64 v[24:25], s[8:9], 0, v[24:25]
	s_mov_b64 s[8:9], 0x8c00e00
	v_lshl_add_u64 v[36:37], v[24:25], 0, s[8:9]
	s_lshl_b64 s[8:9], s[2:3], 12
	s_add_u32 s8, s70, s8
	v_mov_b32_e32 v17, v33
	s_addc_u32 s9, s71, s9
	v_lshl_add_u64 v[16:17], s[8:9], 0, v[16:17]
	s_mov_b64 s[8:9], 0x1000
	v_or_b32_e32 v18, 0x100, v32
	v_or_b32_e32 v20, 0x200, v32
	v_or_b32_e32 v22, 0x300, v32
	v_lshl_add_u64 v[38:39], v[16:17], 0, s[8:9]
	s_mov_b32 s1, s0
	v_mbcnt_lo_u32_b32 v16, -1, 0
	s_mov_b32 s25, -1
	v_mov_b64_e32 v[40:41], s[0:1]
	s_add_i32 s3, 0, 0x20100
	v_lshlrev_b32_e32 v32, 2, v32
	v_lshlrev_b32_e32 v64, 2, v18
	v_lshlrev_b32_e32 v65, 2, v20
	v_lshlrev_b32_e32 v66, 2, v22
	v_mov_b32_e32 v67, 0x358637bd
	s_mov_b32 s24, 0x800000
	s_mov_b64 s[10:11], 0x2000
	v_mbcnt_hi_u32_b32 v68, -1, v16
	v_mov_b64_e32 v[42:43], s[0:1]
	v_mov_b32_e32 v16, 0
	v_mov_b32_e32 v17, v33
	v_mov_b32_e32 v18, v33
	v_mov_b32_e32 v19, v33
	v_mov_b32_e32 v20, v33
	v_mov_b32_e32 v21, v33
	v_mov_b32_e32 v22, v33
	v_mov_b32_e32 v23, v33
	v_mov_b32_e32 v24, v33
	v_mov_b32_e32 v25, v33
	v_mov_b32_e32 v26, v33
	v_mov_b32_e32 v27, v33
	v_mov_b32_e32 v28, v33
	v_mov_b32_e32 v29, v33
	v_mov_b32_e32 v30, v33
	v_mov_b32_e32 v31, v33
	v_lshlrev_b32_e32 v236, 2, v250
	s_ashr_i32 s7, s6, 31
	s_lshl_b64 s[98:99], s[6:7], 2
	s_add_u32 s98, s20, s98
	s_addc_u32 s99, s21, s99
	global_load_dword v237, v236, s[98:99]
	s_mov_b32 s100, 0
	s_waitcnt vmcnt(0)
	s_branch .LBB0_2300
.LBB0_2299:
	s_add_i32 s2, s2, 2
	s_add_i32 s6, s6, 4
	s_add_i32 s100, s100, 4
	v_lshl_add_u64 v[36:37], v[36:37], 0, s[8:9]
	s_cmp_lt_i32 s2, s18
	v_lshl_add_u64 v[38:39], v[38:39], 0, s[10:11]
	s_cbranch_scc0 .LBB0_2310
.LBB0_2300:
	s_ashr_i32 s7, s6, 31
	s_lshl_b64 s[0:1], s[6:7], 2
	s_add_u32 s12, s20, s0
	s_addc_u32 s13, s21, s1
	v_readlane_b32 s98, v237, s100
	s_add_i32 s12, s6, 1
	s_ashr_i32 s13, s12, 31
	s_lshl_b64 s[14:15], s[12:13], 2
	s_add_u32 s12, s20, s14
	s_addc_u32 s13, s21, s15
	s_add_i32 s101, s100, 1
	v_readlane_b32 s99, v237, s101
	s_nop 1
	v_mov_b32_e32 v60, s98
	v_mov_b32_e32 v61, s99
	s_waitcnt vmcnt(1)
	v_ashrrev_i32_e32 v62, 15, v60
	v_lshlrev_b32_e32 v62, 2, v62
	v_add_u32_e32 v62, s3, v62
	ds_read_b32 v62, v62
	v_and_b32_e32 v60, 0x7fff, v60
	s_waitcnt vmcnt(0)
	v_ashrrev_i32_e32 v63, 15, v61
	v_lshlrev_b32_e32 v63, 2, v63
	v_add_u32_e32 v63, s3, v63
	ds_read_b32 v63, v63
	s_waitcnt lgkmcnt(1)
	v_lshlrev_b32_e32 v62, 8, v62
	v_add_u32_e32 v62, v62, v60
	v_and_b32_e32 v61, 0x7fff, v61
	s_waitcnt lgkmcnt(0)
	v_lshlrev_b32_e32 v60, 8, v63
	v_add_u32_e32 v60, v60, v61
	v_max_i32_e32 v61, v62, v60
	v_cmp_le_i32_e32 vcc, s19, v61
	s_or_b64 s[12:13], s[4:5], vcc
	s_and_b64 vcc, exec, s[12:13]
	s_cbranch_vccz .LBB0_2302
	s_add_u32 s0, s22, s0
	v_ashrrev_i32_e32 v63, 31, v62
	s_addc_u32 s1, s23, s1
	v_lshlrev_b64 v[50:51], 10, v[62:63]
	v_ashrrev_i32_e32 v61, 31, v60
	s_add_u32 s14, s22, s14
	v_lshl_add_u64 v[62:63], v[34:35], 0, v[50:51]
	v_lshlrev_b64 v[50:51], 10, v[60:61]
	s_addc_u32 s15, s23, s15
	global_load_dword v40, v33, s[0:1]
	global_load_dword v42, v33, s[14:15]
	v_lshl_add_u64 v[60:61], v[34:35], 0, v[50:51]
	global_load_dwordx2 v[50:51], v[36:37], off offset:-3584
	global_load_dwordx2 v[54:55], v[36:37], off offset:-3072
	global_load_dwordx2 v[56:57], v[36:37], off offset:-2560
	global_load_dwordx2 v[58:59], v[36:37], off offset:-2048
	global_load_dword v72, v[62:63], off
	global_load_dword v81, v[60:61], off
	global_load_dword v74, v[62:63], off offset:256
	global_load_dword v82, v[60:61], off offset:256
	global_load_dword v75, v[62:63], off offset:512
	global_load_dword v83, v[60:61], off offset:512
	global_load_dword v84, v[60:61], off offset:768
	global_load_dword v77, v[62:63], off offset:768
	s_waitcnt vmcnt(13)
	v_mul_f32_e32 v40, 0x3d800000, v40
	s_waitcnt vmcnt(12)
	v_mul_f32_e32 v42, 0x3d800000, v42
.LBB0_2302:
	s_add_i32 s0, s6, 2
	s_ashr_i32 s1, s0, 31
	s_lshl_b64 s[14:15], s[0:1], 2
	s_add_u32 s0, s20, s14
	s_addc_u32 s1, s21, s15
	s_add_i32 s101, s100, 2
	v_readlane_b32 s98, v237, s101
	s_add_i32 s0, s6, 3
	s_ashr_i32 s1, s0, 31
	s_lshl_b64 s[16:17], s[0:1], 2
	s_add_u32 s0, s20, s16
	s_addc_u32 s1, s21, s17
	s_add_i32 s101, s100, 3
	v_readlane_b32 s99, v237, s101
	s_nop 1
	v_mov_b32_e32 v60, s98
	v_mov_b32_e32 v61, s99
	s_waitcnt vmcnt(1)
	v_ashrrev_i32_e32 v62, 15, v60
	v_lshlrev_b32_e32 v62, 2, v62
	v_add_u32_e32 v62, s3, v62
	ds_read_b32 v62, v62
	v_and_b32_e32 v60, 0x7fff, v60
	s_waitcnt vmcnt(0)
	v_ashrrev_i32_e32 v63, 15, v61
	v_lshlrev_b32_e32 v63, 2, v63
	v_add_u32_e32 v63, s3, v63
	ds_read_b32 v63, v63
	s_waitcnt lgkmcnt(1)
	v_lshlrev_b32_e32 v62, 8, v62
	v_and_b32_e32 v61, 0x7fff, v61
	v_add_u32_e32 v62, v62, v60
	s_waitcnt lgkmcnt(0)
	v_lshlrev_b32_e32 v60, 8, v63
	v_add_u32_e32 v60, v60, v61
	v_max_i32_e32 v61, v62, v60
	v_cmp_le_i32_e32 vcc, s19, v61
	s_or_b64 s[26:27], s[4:5], vcc
	v_cndmask_b32_e64 v61, 0, 1, s[26:27]
	v_cmp_ne_u32_e64 s[0:1], 1, v61
	s_andn2_b64 vcc, exec, s[26:27]
	s_cbranch_vccnz .LBB0_2304
	s_add_u32 s14, s22, s14
	v_ashrrev_i32_e32 v63, 31, v62
	s_addc_u32 s15, s23, s15
	v_lshlrev_b64 v[44:45], 10, v[62:63]
	v_ashrrev_i32_e32 v61, 31, v60
	s_add_u32 s16, s22, s16
	v_lshl_add_u64 v[62:63], v[34:35], 0, v[44:45]
	v_lshlrev_b64 v[44:45], 10, v[60:61]
	s_addc_u32 s17, s23, s17
	global_load_dword v41, v33, s[14:15]
	global_load_dword v43, v33, s[16:17]
	v_lshl_add_u64 v[60:61], v[34:35], 0, v[44:45]
	global_load_dwordx2 v[44:45], v[36:37], off offset:-1536
	global_load_dwordx2 v[46:47], v[36:37], off offset:-1024
	global_load_dwordx2 v[48:49], v[36:37], off offset:-512
	global_load_dwordx2 v[52:53], v[36:37], off
	global_load_dword v69, v[62:63], off
	global_load_dword v76, v[60:61], off
	global_load_dword v70, v[62:63], off offset:256
	global_load_dword v78, v[60:61], off offset:256
	global_load_dword v71, v[62:63], off offset:512
	global_load_dword v79, v[60:61], off offset:512
	global_load_dword v80, v[60:61], off offset:768
	global_load_dword v73, v[62:63], off offset:768
	s_waitcnt vmcnt(13)
	v_mul_f32_e32 v41, 0x3d800000, v41
	s_waitcnt vmcnt(12)
	v_mul_f32_e32 v43, 0x3d800000, v43
